# baseline (speedup 1.0000x reference)
_Z11k_proj_mfmaPKDF16_PKDv8_DF16_PKfPfPS1_S6_PhS6_PDF16_:
	v_readfirstlane_b32 s21, v0
	s_lshr_b32 s20, s21, 6
	s_and_b32 s24, s2, 3
	s_cmp_lg_u32 s24, 0
	s_cselect_b64 s[8:9], -1, 0
	s_cmp_eq_u32 s24, 2
	s_cselect_b32 s3, 28, 40
	s_cselect_b32 s4, 40, 50
	s_cmp_eq_u32 s24, 1
	s_cselect_b32 s3, 18, s3
	s_cselect_b32 s10, 28, s4
	s_cmp_eq_u32 s24, 0
	s_cselect_b64 s[4:5], -1, 0
	s_load_dwordx2 s[16:17], s[0:1], 0x8
	s_load_dwordx2 s[30:31], s[0:1], 0x0
	s_and_b64 s[6:7], s[4:5], exec
	s_cselect_b32 s26, 0, s3
	s_cselect_b32 s3, 18, s10
	s_add_i32 s27, s20, s26
	s_waitcnt lgkmcnt(0)
	s_lshr_b32 s36, s2, 2
	s_mul_i32 s36, s36, 0x5000
	s_add_u32 s30, s30, s36
	s_addc_u32 s31, s31, 0
	s_add_u32 s38, s30, 0x2000
	s_addc_u32 s39, s31, 0
	s_add_u32 s40, s30, 0x4000
	s_addc_u32 s41, s31, 0
	v_lshlrev_b32_e32 v1, 4, v0
	s_movk_i32 s36, 0x100
	v_cmp_gt_u32_e32 vcc, s36, v0
	global_load_dwordx4 v[42:45], v1, s[30:31]
	global_load_dwordx4 v[46:49], v1, s[38:39]
	s_and_saveexec_b64 s[42:43], vcc
	global_load_dwordx4 v[50:53], v1, s[40:41]
	s_mov_b64 exec, s[42:43]
	s_cmp_lt_u32 s27, s3
	s_cselect_b64 s[14:15], -1, 0
	s_cmp_ge_u32 s27, s3
	v_and_b32_e32 v146, 63, v0
	s_cbranch_scc1 .LBB2_2
	s_mul_i32 s6, s27, 0x140
	v_or_b32_e32 v2, s6, v146
	v_mov_b32_e32 v3, 0
	s_waitcnt lgkmcnt(0)
	v_lshl_add_u64 v[4:5], v[2:3], 4, s[16:17]
	s_addk_i32 s6, 0x100
	global_load_dwordx4 v[106:109], v[4:5], off
	global_load_dwordx4 v[114:117], v[4:5], off offset:1024
	global_load_dwordx4 v[126:129], v[4:5], off offset:2048
	global_load_dwordx4 v[134:137], v[4:5], off offset:3072
	v_or_b32_e32 v2, s6, v146
	v_lshl_add_u64 v[2:3], v[2:3], 4, s[16:17]
	global_load_dwordx4 v[138:141], v[2:3], off

.LBB2_6:
	v_mul_u32_u24_e32 v1, 0xccd, v0
	s_lshr_b32 s22, s2, 2
	v_lshrrev_b32_e32 v54, 16, v1
	s_waitcnt lgkmcnt(0)
	s_movk_i32 s16, 0xffec
	s_lshl_b32 s25, s22, 6
	v_mad_i32_i24 v55, v54, s16, v0
	v_or_b32_e32 v1, s25, v54
	s_movk_i32 s17, 0x140
	s_lshr_b32 s18, s2, 4
	s_movk_i32 s2, 0x300
	v_or_b32_e32 v1, 0x200, v0
	v_cmp_gt_u32_e32 vcc, s2, v0
	s_load_dwordx2 s[16:17], s[0:1], 0x10
	v_or_b32_e32 v56, 0x400, v0
	s_movk_i32 s2, 0x500
	s_and_b32 s23, s18, 0xffffffc
	v_cmp_gt_u32_e64 s[2:3], s2, v56
	s_waitcnt lgkmcnt(0)
	s_load_dword s23, s[16:17], s23 offset:0x0
	v_lshlrev_b32_e32 v55, 4, v55
	s_movk_i32 s16, 0x150
	v_mad_u32_u24 v54, v54, s16, v55
	s_cmp_lg_u64 s[10:11], 0
	s_cbranch_scc1 .Lmy_pj_w15
	s_cmp_lg_u64 s[12:13], 0
	s_cbranch_scc1 .Lmy_pj_w10
	s_waitcnt vmcnt(5)
	s_branch .Lmy_pj_wd
.Lmy_pj_w10:
	s_waitcnt vmcnt(10)
	s_branch .Lmy_pj_wd
.Lmy_pj_w15:
	s_waitcnt vmcnt(15)
.Lmy_pj_wd:
	ds_write_b128 v54, v[42:45]
	s_and_saveexec_b64 s[6:7], vcc
	s_cbranch_execz .LBB2_12
	v_mul_u32_u24_e32 v42, 0xccd, v1
	v_lshrrev_b32_e32 v42, 16, v42
	v_mul_i32_i24_e32 v43, 0xffffffec, v42
	v_add_lshl_u32 v1, v43, v1, 4
	v_mad_u32_u24 v1, v42, s16, v1
	ds_write_b128 v1, v[46:49]

.LBB2_14:
	s_or_b64 exec, exec, s[6:7]
	v_and_b32_e32 v147, 15, v0
	v_and_b32_e32 v1, 48, v0
	s_movk_i32 s2, 0x150
	v_mad_u32_u24 v1, v147, s2, v1
	s_waitcnt lgkmcnt(0)
	s_barrier
	ds_read_b128 v[130:133], v1
	ds_read_b128 v[122:125], v1 offset:64
	ds_read_b128 v[118:121], v1 offset:128
	ds_read_b128 v[110:113], v1 offset:192
	ds_read_b128 v[102:105], v1 offset:256
	ds_read_b128 v[86:89], v1 offset:5376
	ds_read_b128 v[90:93], v1 offset:5440
	ds_read_b128 v[94:97], v1 offset:5504
	ds_read_b128 v[98:101], v1 offset:5568
	ds_read_b128 v[82:85], v1 offset:5632
	ds_read_b128 v[66:69], v1 offset:10752
	ds_read_b128 v[70:73], v1 offset:10816
	ds_read_b128 v[74:77], v1 offset:10880
	ds_read_b128 v[78:81], v1 offset:10944
	ds_read_b128 v[62:65], v1 offset:11008
	ds_read_b128 v[46:49], v1 offset:16128
	ds_read_b128 v[50:53], v1 offset:16192
	ds_read_b128 v[54:57], v1 offset:16256
	ds_read_b128 v[58:61], v1 offset:16320
	ds_read_b128 v[42:45], v1 offset:16384
	s_waitcnt lgkmcnt(0)
	s_barrier
	s_waitcnt vmcnt(0)
	s_andn2_b64 vcc, exec, s[4:5]
	s_cbranch_vccnz .LBB2_26
	v_sub_u32_e32 v1, 0x83f, v0
	v_lshrrev_b32_e32 v142, 9, v1
	v_add_u32_e32 v1, 4, v142
	v_mov_b32_e32 v148, 0x9480
	v_and_b32_e32 v145, 12, v1
	v_mov_b32_e32 v1, v142
	v_mov_b32_e32 v144, v142
	v_mov_b32_e32 v143, v142
	v_lshl_add_u32 v148, v0, 1, v148
	s_mov_b32 s29, 0
	s_mov_b64 s[16:17], 0
	v_mov_b32_e32 v149, 0
	s_branch .LBB2_17
